# speedup vs baseline: 1.1944x; 1.0327x over previous
.Lrec_step:
	s_bitcmp0_b32 s46, 2
	s_cselect_b32 s28, 0, s34
	s_cselect_b32 s47, s38, s31
	s_cselect_b32 s48, s40, s30
	s_mov_b32 s14, 0
	s_waitcnt vmcnt(5)
	s_cmp_eq_u32 s46, 0
	s_cbranch_scc1 .Lrec_norot
	v_accvgpr_read_b32 v43, a33
	v_accvgpr_read_b32 v42, a32
	v_accvgpr_write_b32 a33, v41
	v_accvgpr_write_b32 a32, v40
.Lrec_norot:
	s_nop 0
	v_fma_mix_f32 v246, v42, s40, v45 op_sel_hi:[1,0,0]
	v_fma_mix_f32 v247, v42, s40, v6 op_sel:[1,0,0] op_sel_hi:[1,0,0]
	v_fma_mix_f32 v248, v43, s38, v8 op_sel_hi:[1,0,0]
	v_fma_mix_f32 v249, v43, s40, v7 op_sel:[1,0,0] op_sel_hi:[1,0,0]
	s_cmp_lg_u32 s46, 0
	s_cbranch_scc1 .Lrec_b0

.Lrec_stored:
	s_cmpk_eq_i32 s14, 0x100
	s_cbranch_scc1 .Lrec_exit
	v_and_or_b32 v15, s29, 56, v56
	v_lshl_add_u32 v15, v15, 6, v0
	ds_write_b16 v15, v14 offset:33024
	v_mov_b32_e32 v44, v12
	v_add_u32_e32 v242, s7, v27
	v_add_u32_e32 v243, s7, v28
	v_add_u32_e32 v244, s7, v29
	v_add_u32_e32 v245, s7, v30
	v_xor_b32_e32 v31, 0x4000, v31
	v_xor_b32_e32 v32, 0x4000, v32
	v_xor_b32_e32 v33, 0x4000, v33
	v_xor_b32_e32 v34, 0x4000, v34
	v_xor_b32_e32 v9, 0x4000, v9
	v_mov_b32_e32 v10, 0
	v_mov_b32_e32 v11, 0
	v_mov_b32_e32 v12, 0
	v_mov_b32_e32 v13, 0
	v_mov_b32_e32 v14, 0
	v_mov_b32_e32 v15, 0
	v_mov_b32_e32 v16, 0
	v_mov_b32_e32 v17, 0
	v_mov_b32_e32 v18, 0
	v_mov_b32_e32 v19, 0
	v_mov_b32_e32 v20, 0
	v_mov_b32_e32 v21, 0
	v_mov_b32_e32 v22, 0
	v_mov_b32_e32 v23, 0
	v_mov_b32_e32 v24, 0
	v_mov_b32_e32 v25, 0
	v_mov_b32_e32 v2, 0
	v_mov_b32_e32 v3, 0
	v_mov_b32_e32 v4, 0
	v_mov_b32_e32 v5, 0
	v_mov_b32_e32 v250, 0
	v_mov_b32_e32 v251, 0
	v_mov_b32_e32 v252, 0
	v_mov_b32_e32 v253, 0
	s_mov_b64 s[26:27], s[24:25]
	v_mov_b32_e32 v46, 0
	v_mov_b32_e32 v47, 0
	v_mov_b32_e32 v48, 0
	v_mov_b32_e32 v49, 0
	v_mov_b32_e32 v50, 0
	v_mov_b32_e32 v51, 0
	v_mov_b32_e32 v52, 0
	v_mov_b32_e32 v53, 0
	s_sleep 2
	buffer_load_dwordx4 v[194:197], v242, s[20:23], 0 offen sc1
	buffer_load_dwordx4 v[198:201], v243, s[20:23], 0 offen sc1
	buffer_load_dwordx4 v[202:205], v244, s[20:23], 0 offen sc1
	buffer_load_dwordx4 v[206:209], v245, s[20:23], 0 offen sc1
	s_cmp_eq_u64 s[2:3], 0
	s_cbranch_scc1 .Lrec_noflush
	s_and_b32 s29, s46, 3
	s_cmp_lg_u32 s29, 0
	s_cbranch_scc1 .Lrec_noflush
	s_cmp_lt_u32 s46, 4
	s_cbranch_scc1 .Lrec_noflush
	s_add_i32 s29, s46, -4
	v_accvgpr_read_b32 v46, a94
	v_or_b32_e32 v50, s29, v46
	v_lshlrev_b32_e32 v46, 3, v50
	v_accvgpr_read_b32 v47, a95
	v_and_or_b32 v46, v46, 40, v47
	v_accvgpr_read_b32 v47, a96
	v_lshl_add_u32 v47, v47, 1, 0
	v_lshl_add_u32 v54, v46, 6, v47
	ds_read_b128 v[46:49], v54 offset:33024
	v_ashrrev_i32_e32 v51, 31, v50
	v_accvgpr_read_b32 v52, a100
	v_lshlrev_b64 v[50:51], 17, v[50:51]
	v_accvgpr_read_b32 v53, a101
	v_lshl_add_u64 v[50:51], v[52:53], 0, v[50:51]
	v_add_co_u32_e32 v52, vcc, 0x20000, v50
	s_nop 1
	v_addc_co_u32_e32 v53, vcc, 0, v51, vcc
	s_waitcnt lgkmcnt(0)
	global_store_dwordx4 v[52:53], v[46:49], off
	s_nop 1
	ds_read_b128 v[46:49], v54 offset:34048
	v_add_co_u32_e32 v50, vcc, 0x60000, v50
	s_nop 1
	v_addc_co_u32_e32 v51, vcc, 0, v51, vcc
	s_waitcnt lgkmcnt(0)
	global_store_dwordx4 v[50:51], v[46:49], off
	s_nop 1
	v_mov_b32_e32 v46, 0
	v_mov_b32_e32 v47, 0
	v_mov_b32_e32 v48, 0
	v_mov_b32_e32 v49, 0
	v_mov_b32_e32 v50, 0
	v_mov_b32_e32 v51, 0
	v_mov_b32_e32 v52, 0
	v_mov_b32_e32 v53, 0
